# v51 + lru_fin_unit: the 8 unrolled items software-pipelined by one item (next item's 3 loads issued before the current item's gelu/combine, own pointers, rotating register sets)
# baseline (speedup 1.0000x reference)
; #define LAS __attribute__((address_space(3)))
; DI float bflo(unsigned w) { return __uint_as_float(w << 16); }
; DI float bfhi(unsigned w) { return __uint_as_float(w & 0xffff0000u); }
; DI u32x2 pack4(f32x4 v) { bf16x4_t r = __builtin_convertvector(v, bf16x4_t); return __builtin_bit_cast(u32x2, r); }
; DI float gelu_tanh(float x) { const float u = 0.7978845608028654f * (x + 0.044715f * x * x * x); const float e = __expf(2.0f * u); const float th = 1.0f - 2.0f / (e + 1.0f); return 0.5f * x * (1.0f + th); }
; DI void lru_fin_unit(const Ctx& c, int u) {
;     ...
;     __syncthreads();
;     const u16* acum = (const u16*)(c.ws + WS_ACUM); const u16* hloc = (const u16*)(c.ws + WS_HLOC); const u16* proj = (const u16*)(c.ws + WS_PROJ); u16* mixed = (u16*)(c.ws + WS_MIXED);
; #pragma unroll
;     for (int it = 0; it < 8; ++it) { const int item = tid + it * NTHR, t = item >> 5, c4 = (item & 31) * 4;
;         const size_t o = (size_t)(t0 + t) * LW + cb + c4;
;         const u32x2 ar = *(const u32x2*)(acum + o), hr = *(const u32x2*)(hloc + o);
;         const f32x4 a = {bflo(ar.x), bfhi(ar.x), bflo(ar.y), bfhi(ar.y)}, hl = {bflo(hr.x), bfhi(hr.x), bflo(hr.y), bfhi(hr.y)}, hi4 = *(const LAS f32x4*)(hin + c4);
;         const u32x2 yb = *(const u32x2*)(proj + (size_t)(t0 + t) * INC + 5 * RW + cb + c4);
;         const float yg[4] = {bflo(yb.x), bfhi(yb.x), bflo(yb.y), bfhi(yb.y)}; f32x4 ov;
; #pragma unroll
;         for (int r = 0; r < 4; ++r) ov[r] = gelu_tanh(yg[r]) * (hl[r] + a[r] * hi4[r]);
;         *(u32x2*)(mixed + (size_t)(t0 + t) * D + RW + cb + c4) = pack4(ov); }
.LBB0_315:
	s_or_b64 exec, exec, s[56:57]
	s_lshl_b32 s6, s45, 7
	s_lshl_b32 s7, s54, 11
	v_lshlrev_b32_e32 v0, 2, v4
	s_or_b32 s8, s6, s7
	v_and_b32_e32 v7, 0x7c, v0
	v_ashrrev_i32_e32 v0, 5, v6
	v_add_u32_e32 v14, s8, v0
	v_ashrrev_i32_e32 v15, 31, v14
	v_lshlrev_b64 v[0:1], 10, v[14:15]
	v_or_b32_e32 v0, v0, v7
	v_lshl_add_u64 v[0:1], v[10:11], 0, v[0:1]
	v_lshlrev_b64 v[0:1], 1, v[0:1]
	v_mov_b64_e32 v[12:13], s[34:35]
	v_lshl_add_u64 v[2:3], s[38:39], 0, v[0:1]
	v_lshl_add_u64 v[0:1], s[48:49], 0, v[0:1]
	v_mad_i64_i32 v[20:21], s[6:7], v14, s59, v[12:13]
	v_lshlrev_b64 v[8:9], 1, v[10:11]
	s_waitcnt lgkmcnt(0)
	s_barrier
	v_mov_b32_e32 v62, 0x8000
	v_mov_b32_e32 v63, 0
	v_mov_b32_e32 v64, 0x30000
	v_mov_b32_e32 v65, 0
	v_mov_b32_e32 v44, v2
	v_mov_b32_e32 v45, v3
	global_load_dwordx2 v[16:17], v[2:3], off
	v_mov_b32_e32 v46, v0
	v_mov_b32_e32 v47, v1
	global_load_dwordx2 v[18:19], v[0:1], off
	v_lshl_add_u64 v[0:1], v[20:21], 0, v[8:9]
	v_lshlrev_b32_e32 v4, 1, v7
	v_lshl_add_u64 v[0:1], v[0:1], 0, v[4:5]
	v_add_co_u32_e32 v0, vcc, s60, v0
	v_lshlrev_b64 v[14:15], 13, v[14:15]
	s_nop 0
	v_addc_co_u32_e32 v1, vcc, 0, v1, vcc
	v_mov_b32_e32 v48, v0
	v_mov_b32_e32 v49, v1
	global_load_dwordx2 v[22:23], v[0:1], off offset:2048
	v_lshl_add_u64 v[44:45], v[44:45], 0, v[62:63]
	global_load_dwordx2 v[56:57], v[44:45], off
	v_lshl_add_u64 v[48:49], v[48:49], 0, v[64:65]
	global_load_dwordx2 v[60:61], v[48:49], off offset:2048
	v_lshl_add_u64 v[46:47], v[46:47], 0, v[62:63]
	global_load_dwordx2 v[58:59], v[46:47], off
	v_lshl_add_u32 v0, v7, 2, 0
	ds_read_b128 v[0:3], v0
	s_add_i32 s63, s63, s44
	s_add_i32 s62, s62, 1
	s_cmpk_gt_i32 s63, 0x1ff
	s_waitcnt vmcnt(5)
	v_lshlrev_b32_e32 v24, 16, v16
	v_and_b32_e32 v25, 0xffff0000, v16
	s_waitcnt vmcnt(4)
	v_lshlrev_b32_e32 v26, 16, v18
	v_and_b32_e32 v27, 0xffff0000, v18
	s_waitcnt lgkmcnt(0)
	v_pk_fma_f32 v[24:25], v[0:1], v[24:25], v[26:27]
	v_lshlrev_b32_e32 v16, 16, v17
	v_and_b32_e32 v17, 0xffff0000, v17
	v_lshlrev_b32_e32 v18, 16, v19
	v_and_b32_e32 v19, 0xffff0000, v19
	v_pk_fma_f32 v[16:17], v[2:3], v[16:17], v[18:19]
	s_waitcnt vmcnt(3)
	v_lshlrev_b32_e32 v28, 16, v22
	v_and_b32_e32 v29, 0xffff0000, v22
	v_lshlrev_b32_e32 v22, 16, v23
	v_and_b32_e32 v23, 0xffff0000, v23
	v_mul_f32_e32 v30, 0x3d372713, v28
	v_mul_f32_e32 v32, 0x3d372713, v29
	v_mov_b32_e32 v31, v28
	v_mov_b32_e32 v33, v29
	v_mul_f32_e32 v34, 0x3d372713, v22
	v_mul_f32_e32 v36, 0x3d372713, v23
	v_mul_f32_e32 v30, v30, v28
	v_mul_f32_e32 v32, v32, v29
	v_mov_b32_e32 v35, v22
	v_mov_b32_e32 v37, v23
	v_mul_f32_e32 v34, v34, v22
	v_mul_f32_e32 v36, v36, v23
	v_fmac_f32_e32 v31, v30, v31
	v_fmac_f32_e32 v33, v32, v33
	v_fmac_f32_e32 v35, v34, v35
	v_fmac_f32_e32 v37, v36, v37
	v_mul_f32_e32 v30, 0x3f4c422a, v31
	v_mul_f32_e32 v31, 0x3f4c422a, v33
	v_mul_f32_e32 v32, 0x3f4c422a, v35
	v_mul_f32_e32 v33, 0x3f4c422a, v37
	v_add_f32_e32 v30, v30, v30
	v_add_f32_e32 v31, v31, v31
	v_add_f32_e32 v32, v32, v32
	v_add_f32_e32 v33, v33, v33
	v_mul_f32_e32 v30, 0x3fb8aa3b, v30
	v_mul_f32_e32 v31, 0x3fb8aa3b, v31
	v_mul_f32_e32 v32, 0x3fb8aa3b, v32
	v_mul_f32_e32 v33, 0x3fb8aa3b, v33
	v_exp_f32_e32 v30, v30
	v_exp_f32_e32 v31, v31
	v_exp_f32_e32 v32, v32
	v_exp_f32_e32 v33, v33
	v_pk_mul_f32 v[28:29], v[28:29], 0.5 op_sel_hi:[1,0]
	v_pk_add_f32 v[26:27], v[30:31], 1.0 op_sel_hi:[1,0]
	v_pk_mul_f32 v[22:23], v[22:23], 0.5 op_sel_hi:[1,0]
	v_pk_add_f32 v[30:31], v[32:33], 1.0 op_sel_hi:[1,0]
	v_div_scale_f32 v32, s[6:7], v27, v27, 2.0
	v_div_scale_f32 v34, s[6:7], v26, v26, 2.0
	v_rcp_f32_e32 v36, v32
	v_div_scale_f32 v35, s[6:7], v31, v31, 2.0
	v_rcp_f32_e32 v37, v34
	v_rcp_f32_e32 v38, v35
	v_fma_f32 v40, -v32, v36, 1.0
	v_div_scale_f32 v33, vcc, 2.0, v27, 2.0
	v_fma_f32 v41, -v34, v37, 1.0
	v_fmac_f32_e32 v36, v40, v36
	v_div_scale_f32 v39, s[6:7], 2.0, v26, 2.0
	v_fma_f32 v42, -v35, v38, 1.0
	v_fmac_f32_e32 v37, v41, v37
	v_mul_f32_e32 v40, v33, v36
	v_fmac_f32_e32 v38, v42, v38
	v_mul_f32_e32 v41, v39, v37
	v_fma_f32 v42, -v32, v40, v33
	v_fma_f32 v43, -v34, v41, v39
	v_fmac_f32_e32 v40, v42, v36
	v_fmac_f32_e32 v41, v43, v37
	v_fma_f32 v32, -v32, v40, v33
	v_fma_f32 v33, -v34, v41, v39
	v_div_fmas_f32 v32, v32, v36, v40
	s_mov_b64 vcc, s[6:7]
	v_div_fixup_f32 v27, v32, v27, 2.0
	v_div_fmas_f32 v32, v33, v37, v41
	v_div_fixup_f32 v26, v32, v26, 2.0
	v_pk_add_f32 v[26:27], v[26:27], 1.0 op_sel_hi:[1,0] neg_lo:[1,0] neg_hi:[1,0]
	s_nop 0
	v_pk_add_f32 v[26:27], v[26:27], 1.0 op_sel_hi:[1,0]
	s_nop 0
	v_pk_mul_f32 v[26:27], v[28:29], v[26:27]
	s_nop 0
	v_pk_mul_f32 v[24:25], v[24:25], v[26:27]
	v_div_scale_f32 v26, vcc, 2.0, v31, 2.0
	v_mul_f32_e32 v27, v26, v38
	v_fma_f32 v28, -v35, v27, v26
	v_fmac_f32_e32 v27, v28, v38
	v_div_scale_f32 v28, s[6:7], v30, v30, 2.0
	v_rcp_f32_e32 v29, v28
	v_fma_f32 v26, -v35, v27, v26
	v_div_fmas_f32 v26, v26, v38, v27
	v_div_fixup_f32 v27, v26, v31, 2.0
	v_fma_f32 v26, -v28, v29, 1.0
	v_fmac_f32_e32 v29, v26, v29
	v_div_scale_f32 v26, vcc, 2.0, v30, 2.0
	v_mul_f32_e32 v31, v26, v29
	v_fma_f32 v32, -v28, v31, v26
	v_fmac_f32_e32 v31, v32, v29
	v_fma_f32 v26, -v28, v31, v26
	v_div_fmas_f32 v26, v26, v29, v31
	v_sub_co_u32_e32 v14, vcc, 0, v14
	v_div_fixup_f32 v26, v26, v30, 2.0
	s_nop 0
	v_subb_co_u32_e32 v15, vcc, 0, v15, vcc
	v_pk_add_f32 v[26:27], v[26:27], 1.0 op_sel_hi:[1,0] neg_lo:[1,0] neg_hi:[1,0]
	v_lshl_add_u64 v[14:15], v[20:21], 0, v[14:15]
	v_pk_add_f32 v[26:27], v[26:27], 1.0 op_sel_hi:[1,0]
	v_lshl_add_u64 v[14:15], v[14:15], 0, v[8:9]
	v_pk_mul_f32 v[22:23], v[22:23], v[26:27]
	v_lshl_add_u64 v[14:15], v[14:15], 0, v[4:5]
	v_pk_mul_f32 v[16:17], v[16:17], v[22:23]
	v_add_co_u32_e32 v14, vcc, s61, v14
	v_cvt_pk_bf16_f32 v17, v16, v17
	v_cvt_pk_bf16_f32 v16, v24, v25
	v_addc_co_u32_e32 v15, vcc, 0, v15, vcc
	global_store_dwordx2 v[14:15], v[16:17], off offset:2048
	v_add_u32_e32 v14, 0x200, v6
	v_ashrrev_i32_e32 v14, 5, v14
	v_add_u32_e32 v14, s8, v14
	v_ashrrev_i32_e32 v15, 31, v14
	v_lshlrev_b64 v[16:17], 10, v[14:15]
	v_or_b32_e32 v16, v16, v7
	v_mad_i64_i32 v[20:21], s[6:7], v14, s59, v[12:13]
	v_lshl_add_u64 v[16:17], v[10:11], 0, v[16:17]
	v_lshl_add_u64 v[22:23], v[20:21], 0, v[8:9]
	v_lshlrev_b64 v[16:17], 1, v[16:17]
	v_lshl_add_u64 v[22:23], v[22:23], 0, v[4:5]
	v_lshl_add_u64 v[18:19], s[38:39], 0, v[16:17]
	v_add_co_u32_e32 v22, vcc, s60, v22
	v_lshl_add_u64 v[16:17], s[48:49], 0, v[16:17]
	s_nop 0
	v_addc_co_u32_e32 v23, vcc, 0, v23, vcc
	v_lshl_add_u64 v[48:49], v[48:49], 0, v[64:65]
	global_load_dwordx2 v[54:55], v[48:49], off offset:2048
	v_lshl_add_u64 v[44:45], v[44:45], 0, v[62:63]
	global_load_dwordx2 v[50:51], v[44:45], off
	v_lshl_add_u64 v[46:47], v[46:47], 0, v[62:63]
	global_load_dwordx2 v[52:53], v[46:47], off
	v_lshlrev_b64 v[14:15], 13, v[14:15]
	s_waitcnt vmcnt(6)
; #define LAS __attribute__((address_space(3)))
; DI float bflo(unsigned w) { return __uint_as_float(w << 16); }
; DI float bfhi(unsigned w) { return __uint_as_float(w & 0xffff0000u); }
; DI u32x2 pack4(f32x4 v) { bf16x4_t r = __builtin_convertvector(v, bf16x4_t); return __builtin_bit_cast(u32x2, r); }
; DI float gelu_tanh(float x) { const float u = 0.7978845608028654f * (x + 0.044715f * x * x * x); const float e = __expf(2.0f * u); const float th = 1.0f - 2.0f / (e + 1.0f); return 0.5f * x * (1.0f + th); }
; DI void lru_fin_unit(const Ctx& c, int u) {
;     ...
;     for (int it = 0; it < 8; ++it) { const int item = tid + it * NTHR, t = item >> 5, c4 = (item & 31) * 4;
;         const size_t o = (size_t)(t0 + t) * LW + cb + c4;
;         const u32x2 ar = *(const u32x2*)(acum + o), hr = *(const u32x2*)(hloc + o);
;         const f32x4 a = {bflo(ar.x), bfhi(ar.x), bflo(ar.y), bfhi(ar.y)}, hl = {bflo(hr.x), bfhi(hr.x), bflo(hr.y), bfhi(hr.y)}, hi4 = *(const LAS f32x4*)(hin + c4);
;         const u32x2 yb = *(const u32x2*)(proj + (size_t)(t0 + t) * INC + 5 * RW + cb + c4);
;         const float yg[4] = {bflo(yb.x), bfhi(yb.x), bflo(yb.y), bfhi(yb.y)}; f32x4 ov;
; #pragma unroll
;         for (int r = 0; r < 4; ++r) ov[r] = gelu_tanh(yg[r]) * (hl[r] + a[r] * hi4[r]);
;         *(u32x2*)(mixed + (size_t)(t0 + t) * D + RW + cb + c4) = pack4(ov); }
	v_lshlrev_b32_e32 v18, 16, v56
	s_waitcnt vmcnt(5)
	v_lshlrev_b32_e32 v22, 16, v60
	v_and_b32_e32 v23, 0xffff0000, v60
	v_mul_f32_e32 v19, 0x3d372713, v22
	v_mul_f32_e32 v28, 0x3d372713, v23
	v_mov_b32_e32 v26, v22
	v_mov_b32_e32 v29, v23
	v_mul_f32_e32 v19, v19, v22
	v_mul_f32_e32 v28, v28, v23
	v_fmac_f32_e32 v26, v19, v26
	v_fmac_f32_e32 v29, v28, v29
	v_mul_f32_e32 v19, 0x3f4c422a, v26
	v_mul_f32_e32 v26, 0x3f4c422a, v29
	v_add_f32_e32 v19, v19, v19
	v_add_f32_e32 v26, v26, v26
	v_mul_f32_e32 v19, 0x3fb8aa3b, v19
	v_mul_f32_e32 v26, 0x3fb8aa3b, v26
	v_exp_f32_e32 v28, v19
	v_exp_f32_e32 v29, v26
	s_waitcnt vmcnt(4)
	v_lshlrev_b32_e32 v30, 16, v58
	v_and_b32_e32 v31, 0xffff0000, v58
	v_and_b32_e32 v19, 0xffff0000, v56
	v_pk_add_f32 v[28:29], v[28:29], 1.0 op_sel_hi:[1,0]
	v_pk_mul_f32 v[22:23], v[22:23], 0.5 op_sel_hi:[1,0]
	v_div_scale_f32 v16, s[6:7], v29, v29, 2.0
	v_rcp_f32_e32 v32, v16
	v_div_scale_f32 v26, s[6:7], v28, v28, 2.0
	v_rcp_f32_e32 v33, v26
	v_fma_f32 v35, -v16, v32, 1.0
	v_div_scale_f32 v24, vcc, 2.0, v29, 2.0
	v_fmac_f32_e32 v32, v35, v32
	v_mul_f32_e32 v35, v24, v32
	v_fma_f32 v37, -v16, v35, v24
	v_fma_f32 v36, -v26, v33, 1.0
	v_fmac_f32_e32 v35, v37, v32
	v_div_scale_f32 v34, s[6:7], 2.0, v28, 2.0
	v_fmac_f32_e32 v33, v36, v33
	v_fma_f32 v16, -v16, v35, v24
	v_mul_f32_e32 v36, v34, v33
	v_div_fmas_f32 v16, v16, v32, v35
	v_div_fixup_f32 v29, v16, v29, 2.0
	v_fma_f32 v16, -v26, v36, v34
	v_fmac_f32_e32 v36, v16, v33
	v_fma_f32 v16, -v26, v36, v34
	s_mov_b64 vcc, s[6:7]
	v_div_fmas_f32 v16, v16, v33, v36
	v_lshlrev_b32_e32 v26, 16, v61
	v_div_fixup_f32 v28, v16, v28, 2.0
	v_mul_f32_e32 v16, 0x3d372713, v26
	v_mul_f32_e32 v16, v16, v26
	v_mov_b32_e32 v24, v26
	v_fmac_f32_e32 v24, v16, v24
	v_mul_f32_e32 v16, 0x3f4c422a, v24
	v_pk_add_f32 v[28:29], v[28:29], 1.0 op_sel_hi:[1,0] neg_lo:[1,0] neg_hi:[1,0]
	v_add_f32_e32 v16, v16, v16
	v_pk_add_f32 v[28:29], v[28:29], 1.0 op_sel_hi:[1,0]
	v_and_b32_e32 v27, 0xffff0000, v61
	v_mul_f32_e32 v16, 0x3fb8aa3b, v16
	v_pk_mul_f32 v[22:23], v[22:23], v[28:29]
	v_exp_f32_e32 v28, v16
	v_mul_f32_e32 v16, 0x3d372713, v27
	v_mul_f32_e32 v16, v16, v27
	v_mov_b32_e32 v24, v27
	v_fmac_f32_e32 v24, v16, v24
	v_mul_f32_e32 v16, 0x3f4c422a, v24
	v_add_f32_e32 v16, v16, v16
	v_mul_f32_e32 v16, 0x3fb8aa3b, v16
	v_exp_f32_e32 v29, v16
	v_pk_fma_f32 v[18:19], v[0:1], v[18:19], v[30:31]
	v_lshlrev_b32_e32 v16, 16, v59
	v_pk_mul_f32 v[18:19], v[18:19], v[22:23]
	v_pk_add_f32 v[28:29], v[28:29], 1.0 op_sel_hi:[1,0]
	v_lshlrev_b32_e32 v22, 16, v57
	v_div_scale_f32 v24, s[6:7], v29, v29, 2.0
	v_rcp_f32_e32 v30, v24
	v_and_b32_e32 v23, 0xffff0000, v57
	v_and_b32_e32 v17, 0xffff0000, v59
	v_pk_mul_f32 v[26:27], v[26:27], 0.5 op_sel_hi:[1,0]
	v_fma_f32 v25, -v24, v30, 1.0
	v_fmac_f32_e32 v30, v25, v30
	v_div_scale_f32 v25, vcc, 2.0, v29, 2.0
	v_mul_f32_e32 v31, v25, v30
	v_fma_f32 v32, -v24, v31, v25
	v_fmac_f32_e32 v31, v32, v30
	v_div_scale_f32 v32, s[6:7], v28, v28, 2.0
	v_rcp_f32_e32 v33, v32
	v_fma_f32 v24, -v24, v31, v25
	v_div_fmas_f32 v24, v24, v30, v31
	v_div_fixup_f32 v25, v24, v29, 2.0
	v_fma_f32 v24, -v32, v33, 1.0
	v_fmac_f32_e32 v33, v24, v33
	v_div_scale_f32 v24, vcc, 2.0, v28, 2.0
	v_mul_f32_e32 v29, v24, v33
	v_fma_f32 v30, -v32, v29, v24
	v_fmac_f32_e32 v29, v30, v33
	v_fma_f32 v24, -v32, v29, v24
	v_div_fmas_f32 v24, v24, v33, v29
	v_sub_co_u32_e32 v14, vcc, 0, v14
	v_div_fixup_f32 v24, v24, v28, 2.0
	s_nop 0
	v_subb_co_u32_e32 v15, vcc, 0, v15, vcc
	v_pk_add_f32 v[24:25], v[24:25], 1.0 op_sel_hi:[1,0] neg_lo:[1,0] neg_hi:[1,0]
	v_lshl_add_u64 v[14:15], v[20:21], 0, v[14:15]
	v_pk_add_f32 v[24:25], v[24:25], 1.0 op_sel_hi:[1,0]
	v_lshl_add_u64 v[14:15], v[14:15], 0, v[8:9]
	v_pk_mul_f32 v[24:25], v[26:27], v[24:25]
	v_pk_fma_f32 v[16:17], v[2:3], v[22:23], v[16:17]
	v_lshl_add_u64 v[14:15], v[14:15], 0, v[4:5]
	v_pk_mul_f32 v[16:17], v[16:17], v[24:25]
	v_add_co_u32_e32 v14, vcc, s61, v14
	v_cvt_pk_bf16_f32 v17, v16, v17
	v_cvt_pk_bf16_f32 v16, v18, v19
	v_addc_co_u32_e32 v15, vcc, 0, v15, vcc
	global_store_dwordx2 v[14:15], v[16:17], off offset:2048
	v_add_u32_e32 v14, 0x400, v6
	v_ashrrev_i32_e32 v14, 5, v14
	v_add_u32_e32 v14, s8, v14
	v_mad_i64_i32 v[16:17], s[6:7], v14, s59, v[12:13]
	v_lshl_add_u64 v[18:19], v[16:17], 0, v[8:9]
	v_lshl_add_u64 v[18:19], v[18:19], 0, v[4:5]
	v_add_co_u32_e32 v18, vcc, s60, v18
	v_ashrrev_i32_e32 v15, 31, v14
	s_nop 0
	v_addc_co_u32_e32 v19, vcc, 0, v19, vcc
	v_lshl_add_u64 v[48:49], v[48:49], 0, v[64:65]
	global_load_dwordx2 v[60:61], v[48:49], off offset:2048
	v_lshl_add_u64 v[44:45], v[44:45], 0, v[62:63]
	global_load_dwordx2 v[56:57], v[44:45], off
	v_lshl_add_u64 v[46:47], v[46:47], 0, v[62:63]
	global_load_dwordx2 v[58:59], v[46:47], off
	v_lshlrev_b64 v[20:21], 10, v[14:15]
	v_or_b32_e32 v20, v20, v7
	v_lshl_add_u64 v[20:21], v[10:11], 0, v[20:21]
	v_lshlrev_b64 v[20:21], 1, v[20:21]
	v_lshl_add_u64 v[22:23], s[38:39], 0, v[20:21]
	v_lshl_add_u64 v[20:21], s[48:49], 0, v[20:21]
	v_lshlrev_b64 v[14:15], 13, v[14:15]
	s_waitcnt vmcnt(6)
	v_lshlrev_b32_e32 v24, 16, v54
	v_and_b32_e32 v25, 0xffff0000, v54
	v_mul_f32_e32 v18, 0x3d372713, v24
	v_mul_f32_e32 v18, v18, v24
	v_mov_b32_e32 v26, v24
	v_fmac_f32_e32 v26, v18, v26
	v_mul_f32_e32 v18, 0x3f4c422a, v26
	v_add_f32_e32 v18, v18, v18
	v_mul_f32_e32 v18, 0x3fb8aa3b, v18
	v_exp_f32_e32 v26, v18
	v_mul_f32_e32 v18, 0x3d372713, v25
	v_mul_f32_e32 v18, v18, v25
	v_mov_b32_e32 v27, v25
	v_fmac_f32_e32 v27, v18, v27
	v_mul_f32_e32 v18, 0x3f4c422a, v27
	v_add_f32_e32 v18, v18, v18
	v_mul_f32_e32 v18, 0x3fb8aa3b, v18
	v_exp_f32_e32 v27, v18
	s_waitcnt vmcnt(4)
; #define LAS __attribute__((address_space(3)))
; DI float bflo(unsigned w) { return __uint_as_float(w << 16); }
; DI float bfhi(unsigned w) { return __uint_as_float(w & 0xffff0000u); }
; DI u32x2 pack4(f32x4 v) { bf16x4_t r = __builtin_convertvector(v, bf16x4_t); return __builtin_bit_cast(u32x2, r); }
; DI float gelu_tanh(float x) { const float u = 0.7978845608028654f * (x + 0.044715f * x * x * x); const float e = __expf(2.0f * u); const float th = 1.0f - 2.0f / (e + 1.0f); return 0.5f * x * (1.0f + th); }
; DI void lru_fin_unit(const Ctx& c, int u) {
;     ...
;     for (int it = 0; it < 8; ++it) { const int item = tid + it * NTHR, t = item >> 5, c4 = (item & 31) * 4;
;         const size_t o = (size_t)(t0 + t) * LW + cb + c4;
;         const u32x2 ar = *(const u32x2*)(acum + o), hr = *(const u32x2*)(hloc + o);
;         const f32x4 a = {bflo(ar.x), bfhi(ar.x), bflo(ar.y), bfhi(ar.y)}, hl = {bflo(hr.x), bfhi(hr.x), bflo(hr.y), bfhi(hr.y)}, hi4 = *(const LAS f32x4*)(hin + c4);
;         const u32x2 yb = *(const u32x2*)(proj + (size_t)(t0 + t) * INC + 5 * RW + cb + c4);
;         const float yg[4] = {bflo(yb.x), bfhi(yb.x), bflo(yb.y), bfhi(yb.y)}; f32x4 ov;
; #pragma unroll
;         for (int r = 0; r < 4; ++r) ov[r] = gelu_tanh(yg[r]) * (hl[r] + a[r] * hi4[r]);
;         *(u32x2*)(mixed + (size_t)(t0 + t) * D + RW + cb + c4) = pack4(ov); }
	v_lshlrev_b32_e32 v30, 16, v52
	v_and_b32_e32 v31, 0xffff0000, v52
	v_lshlrev_b32_e32 v28, 16, v50
	v_pk_add_f32 v[26:27], v[26:27], 1.0 op_sel_hi:[1,0]
	v_and_b32_e32 v29, 0xffff0000, v50
	v_div_scale_f32 v18, s[6:7], v27, v27, 2.0
	v_rcp_f32_e32 v32, v18
	v_pk_mul_f32 v[24:25], v[24:25], 0.5 op_sel_hi:[1,0]
	v_pk_fma_f32 v[28:29], v[0:1], v[28:29], v[30:31]
	v_fma_f32 v20, -v18, v32, 1.0
	v_fmac_f32_e32 v32, v20, v32
	v_div_scale_f32 v20, vcc, 2.0, v27, 2.0
	v_mul_f32_e32 v22, v20, v32
	v_fma_f32 v33, -v18, v22, v20
	v_fmac_f32_e32 v22, v33, v32
	v_fma_f32 v18, -v18, v22, v20
	v_div_scale_f32 v20, s[6:7], v26, v26, 2.0
	v_rcp_f32_e32 v33, v20
	v_div_fmas_f32 v18, v18, v32, v22
	v_div_fixup_f32 v27, v18, v27, 2.0
	v_fma_f32 v18, -v20, v33, 1.0
	v_fmac_f32_e32 v33, v18, v33
	v_div_scale_f32 v18, vcc, 2.0, v26, 2.0
	v_mul_f32_e32 v22, v18, v33
	v_fma_f32 v32, -v20, v22, v18
	v_fmac_f32_e32 v22, v32, v33
	v_fma_f32 v18, -v20, v22, v18
	v_div_fmas_f32 v18, v18, v33, v22
	v_div_fixup_f32 v26, v18, v26, 2.0
	v_lshlrev_b32_e32 v18, 16, v55
	v_mul_f32_e32 v20, 0x3d372713, v18
	v_mul_f32_e32 v20, v20, v18
	v_mov_b32_e32 v22, v18
	v_fmac_f32_e32 v22, v20, v22
	v_mul_f32_e32 v20, 0x3f4c422a, v22
	v_pk_add_f32 v[26:27], v[26:27], 1.0 op_sel_hi:[1,0] neg_lo:[1,0] neg_hi:[1,0]
	v_add_f32_e32 v20, v20, v20
	v_pk_add_f32 v[26:27], v[26:27], 1.0 op_sel_hi:[1,0]
	v_and_b32_e32 v19, 0xffff0000, v55
	v_mul_f32_e32 v20, 0x3fb8aa3b, v20
	v_pk_mul_f32 v[24:25], v[24:25], v[26:27]
	v_exp_f32_e32 v26, v20
	v_mul_f32_e32 v20, 0x3d372713, v19
	v_mul_f32_e32 v20, v20, v19
	v_mov_b32_e32 v22, v19
	v_fmac_f32_e32 v22, v20, v22
	v_mul_f32_e32 v20, 0x3f4c422a, v22
	v_add_f32_e32 v20, v20, v20
	v_mul_f32_e32 v20, 0x3fb8aa3b, v20
	v_exp_f32_e32 v27, v20
	v_pk_mul_f32 v[24:25], v[28:29], v[24:25]
	v_lshlrev_b32_e32 v22, 16, v51
	v_and_b32_e32 v23, 0xffff0000, v51
	v_pk_add_f32 v[26:27], v[26:27], 1.0 op_sel_hi:[1,0]
	v_lshlrev_b32_e32 v20, 16, v53
	v_div_scale_f32 v28, s[6:7], v27, v27, 2.0
	v_rcp_f32_e32 v29, v28
	v_and_b32_e32 v21, 0xffff0000, v53
	v_pk_mul_f32 v[18:19], v[18:19], 0.5 op_sel_hi:[1,0]
	v_pk_fma_f32 v[20:21], v[2:3], v[22:23], v[20:21]
	v_fma_f32 v30, -v28, v29, 1.0
	v_fmac_f32_e32 v29, v30, v29
	v_div_scale_f32 v30, vcc, 2.0, v27, 2.0
	v_mul_f32_e32 v31, v30, v29
	v_fma_f32 v32, -v28, v31, v30
	v_fmac_f32_e32 v31, v32, v29
	v_fma_f32 v28, -v28, v31, v30
	v_div_scale_f32 v30, s[6:7], v26, v26, 2.0
	v_rcp_f32_e32 v32, v30
	v_div_fmas_f32 v28, v28, v29, v31
	v_div_fixup_f32 v27, v28, v27, 2.0
	v_fma_f32 v28, -v30, v32, 1.0
	v_fmac_f32_e32 v32, v28, v32
	v_div_scale_f32 v28, vcc, 2.0, v26, 2.0
	v_mul_f32_e32 v29, v28, v32
	v_fma_f32 v31, -v30, v29, v28
	v_fmac_f32_e32 v29, v31, v32
	v_fma_f32 v28, -v30, v29, v28
	v_div_fmas_f32 v28, v28, v32, v29
	v_sub_co_u32_e32 v14, vcc, 0, v14
	v_div_fixup_f32 v26, v28, v26, 2.0
	s_nop 0
	v_subb_co_u32_e32 v15, vcc, 0, v15, vcc
	v_pk_add_f32 v[26:27], v[26:27], 1.0 op_sel_hi:[1,0] neg_lo:[1,0] neg_hi:[1,0]
	v_lshl_add_u64 v[14:15], v[16:17], 0, v[14:15]
	v_pk_add_f32 v[26:27], v[26:27], 1.0 op_sel_hi:[1,0]
	v_lshl_add_u64 v[14:15], v[14:15], 0, v[8:9]
	v_pk_mul_f32 v[18:19], v[18:19], v[26:27]
	v_lshl_add_u64 v[14:15], v[14:15], 0, v[4:5]
	v_pk_mul_f32 v[18:19], v[20:21], v[18:19]
	v_add_co_u32_e32 v14, vcc, s61, v14
	v_cvt_pk_bf16_f32 v19, v18, v19
	v_cvt_pk_bf16_f32 v18, v24, v25
	v_addc_co_u32_e32 v15, vcc, 0, v15, vcc
	global_store_dwordx2 v[14:15], v[18:19], off offset:2048
	v_add_u32_e32 v14, 0x600, v6
	v_ashrrev_i32_e32 v14, 5, v14
	v_add_u32_e32 v14, s8, v14
	v_mad_i64_i32 v[16:17], s[6:7], v14, s59, v[12:13]
	v_lshl_add_u64 v[18:19], v[16:17], 0, v[8:9]
	v_lshl_add_u64 v[18:19], v[18:19], 0, v[4:5]
	v_add_co_u32_e32 v18, vcc, s60, v18
	v_ashrrev_i32_e32 v15, 31, v14
	s_nop 0
	v_addc_co_u32_e32 v19, vcc, 0, v19, vcc
	v_lshl_add_u64 v[48:49], v[48:49], 0, v[64:65]
	global_load_dwordx2 v[54:55], v[48:49], off offset:2048
	v_lshl_add_u64 v[44:45], v[44:45], 0, v[62:63]
	global_load_dwordx2 v[50:51], v[44:45], off
	v_lshl_add_u64 v[46:47], v[46:47], 0, v[62:63]
	global_load_dwordx2 v[52:53], v[46:47], off
	v_lshlrev_b64 v[20:21], 10, v[14:15]
	v_or_b32_e32 v20, v20, v7
	v_lshl_add_u64 v[20:21], v[10:11], 0, v[20:21]
	v_lshlrev_b64 v[20:21], 1, v[20:21]
	v_lshl_add_u64 v[22:23], s[38:39], 0, v[20:21]
	v_lshl_add_u64 v[20:21], s[48:49], 0, v[20:21]
	v_lshlrev_b64 v[14:15], 13, v[14:15]
	s_waitcnt vmcnt(6)
	v_lshlrev_b32_e32 v24, 16, v60
	v_and_b32_e32 v25, 0xffff0000, v60
	v_mul_f32_e32 v18, 0x3d372713, v24
	v_mul_f32_e32 v18, v18, v24
	v_mov_b32_e32 v26, v24
	v_fmac_f32_e32 v26, v18, v26
	v_mul_f32_e32 v18, 0x3f4c422a, v26
	v_add_f32_e32 v18, v18, v18
	v_mul_f32_e32 v18, 0x3fb8aa3b, v18
	v_exp_f32_e32 v26, v18
	v_mul_f32_e32 v18, 0x3d372713, v25
	v_mul_f32_e32 v18, v18, v25
	v_mov_b32_e32 v27, v25
	v_fmac_f32_e32 v27, v18, v27
	v_mul_f32_e32 v18, 0x3f4c422a, v27
	v_add_f32_e32 v18, v18, v18
	v_mul_f32_e32 v18, 0x3fb8aa3b, v18
	v_exp_f32_e32 v27, v18
	s_waitcnt vmcnt(4)
; #define LAS __attribute__((address_space(3)))
; DI float bflo(unsigned w) { return __uint_as_float(w << 16); }
; DI float bfhi(unsigned w) { return __uint_as_float(w & 0xffff0000u); }
; DI u32x2 pack4(f32x4 v) { bf16x4_t r = __builtin_convertvector(v, bf16x4_t); return __builtin_bit_cast(u32x2, r); }
; DI float gelu_tanh(float x) { const float u = 0.7978845608028654f * (x + 0.044715f * x * x * x); const float e = __expf(2.0f * u); const float th = 1.0f - 2.0f / (e + 1.0f); return 0.5f * x * (1.0f + th); }
; DI void lru_fin_unit(const Ctx& c, int u) {
;     ...
;     for (int it = 0; it < 8; ++it) { const int item = tid + it * NTHR, t = item >> 5, c4 = (item & 31) * 4;
;         const size_t o = (size_t)(t0 + t) * LW + cb + c4;
;         const u32x2 ar = *(const u32x2*)(acum + o), hr = *(const u32x2*)(hloc + o);
;         const f32x4 a = {bflo(ar.x), bfhi(ar.x), bflo(ar.y), bfhi(ar.y)}, hl = {bflo(hr.x), bfhi(hr.x), bflo(hr.y), bfhi(hr.y)}, hi4 = *(const LAS f32x4*)(hin + c4);
;         const u32x2 yb = *(const u32x2*)(proj + (size_t)(t0 + t) * INC + 5 * RW + cb + c4);
;         const float yg[4] = {bflo(yb.x), bfhi(yb.x), bflo(yb.y), bfhi(yb.y)}; f32x4 ov;
; #pragma unroll
;         for (int r = 0; r < 4; ++r) ov[r] = gelu_tanh(yg[r]) * (hl[r] + a[r] * hi4[r]);
;         *(u32x2*)(mixed + (size_t)(t0 + t) * D + RW + cb + c4) = pack4(ov); }
	v_lshlrev_b32_e32 v30, 16, v58
	v_and_b32_e32 v31, 0xffff0000, v58
	v_lshlrev_b32_e32 v28, 16, v56
	v_pk_add_f32 v[26:27], v[26:27], 1.0 op_sel_hi:[1,0]
	v_and_b32_e32 v29, 0xffff0000, v56
	v_div_scale_f32 v18, s[6:7], v27, v27, 2.0
	v_rcp_f32_e32 v32, v18
	v_pk_mul_f32 v[24:25], v[24:25], 0.5 op_sel_hi:[1,0]
	v_pk_fma_f32 v[28:29], v[0:1], v[28:29], v[30:31]
	v_fma_f32 v20, -v18, v32, 1.0
	v_fmac_f32_e32 v32, v20, v32
	v_div_scale_f32 v20, vcc, 2.0, v27, 2.0
	v_mul_f32_e32 v22, v20, v32
	v_fma_f32 v33, -v18, v22, v20
	v_fmac_f32_e32 v22, v33, v32
	v_fma_f32 v18, -v18, v22, v20
	v_div_scale_f32 v20, s[6:7], v26, v26, 2.0
	v_rcp_f32_e32 v33, v20
	v_div_fmas_f32 v18, v18, v32, v22
	v_div_fixup_f32 v27, v18, v27, 2.0
	v_fma_f32 v18, -v20, v33, 1.0
	v_fmac_f32_e32 v33, v18, v33
	v_div_scale_f32 v18, vcc, 2.0, v26, 2.0
	v_mul_f32_e32 v22, v18, v33
	v_fma_f32 v32, -v20, v22, v18
	v_fmac_f32_e32 v22, v32, v33
	v_fma_f32 v18, -v20, v22, v18
	v_div_fmas_f32 v18, v18, v33, v22
	v_div_fixup_f32 v26, v18, v26, 2.0
	v_lshlrev_b32_e32 v18, 16, v61
	v_mul_f32_e32 v20, 0x3d372713, v18
	v_mul_f32_e32 v20, v20, v18
	v_mov_b32_e32 v22, v18
	v_fmac_f32_e32 v22, v20, v22
	v_mul_f32_e32 v20, 0x3f4c422a, v22
	v_pk_add_f32 v[26:27], v[26:27], 1.0 op_sel_hi:[1,0] neg_lo:[1,0] neg_hi:[1,0]
	v_add_f32_e32 v20, v20, v20
	v_pk_add_f32 v[26:27], v[26:27], 1.0 op_sel_hi:[1,0]
	v_and_b32_e32 v19, 0xffff0000, v61
	v_mul_f32_e32 v20, 0x3fb8aa3b, v20
	v_pk_mul_f32 v[24:25], v[24:25], v[26:27]
	v_exp_f32_e32 v26, v20
	v_mul_f32_e32 v20, 0x3d372713, v19
	v_mul_f32_e32 v20, v20, v19
	v_mov_b32_e32 v22, v19
	v_fmac_f32_e32 v22, v20, v22
	v_mul_f32_e32 v20, 0x3f4c422a, v22
	v_add_f32_e32 v20, v20, v20
	v_mul_f32_e32 v20, 0x3fb8aa3b, v20
	v_exp_f32_e32 v27, v20
	v_pk_mul_f32 v[24:25], v[28:29], v[24:25]
	v_lshlrev_b32_e32 v22, 16, v57
	v_and_b32_e32 v23, 0xffff0000, v57
	v_pk_add_f32 v[26:27], v[26:27], 1.0 op_sel_hi:[1,0]
	v_lshlrev_b32_e32 v20, 16, v59
	v_div_scale_f32 v28, s[6:7], v27, v27, 2.0
	v_rcp_f32_e32 v29, v28
	v_and_b32_e32 v21, 0xffff0000, v59
	v_pk_mul_f32 v[18:19], v[18:19], 0.5 op_sel_hi:[1,0]
	v_pk_fma_f32 v[20:21], v[2:3], v[22:23], v[20:21]
	v_fma_f32 v30, -v28, v29, 1.0
	v_fmac_f32_e32 v29, v30, v29
	v_div_scale_f32 v30, vcc, 2.0, v27, 2.0
	v_mul_f32_e32 v31, v30, v29
	v_fma_f32 v32, -v28, v31, v30
	v_fmac_f32_e32 v31, v32, v29
	v_fma_f32 v28, -v28, v31, v30
	v_div_scale_f32 v30, s[6:7], v26, v26, 2.0
	v_rcp_f32_e32 v32, v30
	v_div_fmas_f32 v28, v28, v29, v31
	v_div_fixup_f32 v27, v28, v27, 2.0
	v_fma_f32 v28, -v30, v32, 1.0
	v_fmac_f32_e32 v32, v28, v32
	v_div_scale_f32 v28, vcc, 2.0, v26, 2.0
	v_mul_f32_e32 v29, v28, v32
	v_fma_f32 v31, -v30, v29, v28
	v_fmac_f32_e32 v29, v31, v32
	v_fma_f32 v28, -v30, v29, v28
	v_div_fmas_f32 v28, v28, v32, v29
	v_sub_co_u32_e32 v14, vcc, 0, v14
	v_div_fixup_f32 v26, v28, v26, 2.0
	s_nop 0
	v_subb_co_u32_e32 v15, vcc, 0, v15, vcc
	v_pk_add_f32 v[26:27], v[26:27], 1.0 op_sel_hi:[1,0] neg_lo:[1,0] neg_hi:[1,0]
	v_lshl_add_u64 v[14:15], v[16:17], 0, v[14:15]
	v_pk_add_f32 v[26:27], v[26:27], 1.0 op_sel_hi:[1,0]
	v_lshl_add_u64 v[14:15], v[14:15], 0, v[8:9]
	v_pk_mul_f32 v[18:19], v[18:19], v[26:27]
	v_lshl_add_u64 v[14:15], v[14:15], 0, v[4:5]
	v_pk_mul_f32 v[18:19], v[20:21], v[18:19]
	v_add_co_u32_e32 v14, vcc, s61, v14
	v_cvt_pk_bf16_f32 v19, v18, v19
	v_cvt_pk_bf16_f32 v18, v24, v25
	v_addc_co_u32_e32 v15, vcc, 0, v15, vcc
	global_store_dwordx2 v[14:15], v[18:19], off offset:2048
	v_add_u32_e32 v14, 0x800, v6
	v_ashrrev_i32_e32 v14, 5, v14
	v_add_u32_e32 v14, s8, v14
	v_mad_i64_i32 v[16:17], s[6:7], v14, s59, v[12:13]
	v_lshl_add_u64 v[18:19], v[16:17], 0, v[8:9]
	v_lshl_add_u64 v[18:19], v[18:19], 0, v[4:5]
	v_add_co_u32_e32 v18, vcc, s60, v18
	v_ashrrev_i32_e32 v15, 31, v14
	s_nop 0
	v_addc_co_u32_e32 v19, vcc, 0, v19, vcc
	v_lshl_add_u64 v[48:49], v[48:49], 0, v[64:65]
	global_load_dwordx2 v[60:61], v[48:49], off offset:2048
	v_lshl_add_u64 v[44:45], v[44:45], 0, v[62:63]
	global_load_dwordx2 v[56:57], v[44:45], off
	v_lshl_add_u64 v[46:47], v[46:47], 0, v[62:63]
	global_load_dwordx2 v[58:59], v[46:47], off
	v_lshlrev_b64 v[20:21], 10, v[14:15]
	v_or_b32_e32 v20, v20, v7
	v_lshl_add_u64 v[20:21], v[10:11], 0, v[20:21]
	v_lshlrev_b64 v[20:21], 1, v[20:21]
	v_lshl_add_u64 v[22:23], s[38:39], 0, v[20:21]
	v_lshl_add_u64 v[20:21], s[48:49], 0, v[20:21]
	v_lshlrev_b64 v[14:15], 13, v[14:15]
	s_waitcnt vmcnt(6)
	v_lshlrev_b32_e32 v24, 16, v54
	v_and_b32_e32 v25, 0xffff0000, v54
	v_mul_f32_e32 v18, 0x3d372713, v24
	v_mul_f32_e32 v18, v18, v24
	v_mov_b32_e32 v26, v24
	v_fmac_f32_e32 v26, v18, v26
	v_mul_f32_e32 v18, 0x3f4c422a, v26
	v_add_f32_e32 v18, v18, v18
	v_mul_f32_e32 v18, 0x3fb8aa3b, v18
	v_exp_f32_e32 v26, v18
	v_mul_f32_e32 v18, 0x3d372713, v25
	v_mul_f32_e32 v18, v18, v25
	v_mov_b32_e32 v27, v25
	v_fmac_f32_e32 v27, v18, v27
	v_mul_f32_e32 v18, 0x3f4c422a, v27
	v_add_f32_e32 v18, v18, v18
	v_mul_f32_e32 v18, 0x3fb8aa3b, v18
	v_exp_f32_e32 v27, v18
	s_waitcnt vmcnt(4)
; #define LAS __attribute__((address_space(3)))
; DI float bflo(unsigned w) { return __uint_as_float(w << 16); }
; DI float bfhi(unsigned w) { return __uint_as_float(w & 0xffff0000u); }
; DI u32x2 pack4(f32x4 v) { bf16x4_t r = __builtin_convertvector(v, bf16x4_t); return __builtin_bit_cast(u32x2, r); }
; DI float gelu_tanh(float x) { const float u = 0.7978845608028654f * (x + 0.044715f * x * x * x); const float e = __expf(2.0f * u); const float th = 1.0f - 2.0f / (e + 1.0f); return 0.5f * x * (1.0f + th); }
; DI void lru_fin_unit(const Ctx& c, int u) {
;     ...
;     for (int it = 0; it < 8; ++it) { const int item = tid + it * NTHR, t = item >> 5, c4 = (item & 31) * 4;
;         const size_t o = (size_t)(t0 + t) * LW + cb + c4;
;         const u32x2 ar = *(const u32x2*)(acum + o), hr = *(const u32x2*)(hloc + o);
;         const f32x4 a = {bflo(ar.x), bfhi(ar.x), bflo(ar.y), bfhi(ar.y)}, hl = {bflo(hr.x), bfhi(hr.x), bflo(hr.y), bfhi(hr.y)}, hi4 = *(const LAS f32x4*)(hin + c4);
;         const u32x2 yb = *(const u32x2*)(proj + (size_t)(t0 + t) * INC + 5 * RW + cb + c4);
;         const float yg[4] = {bflo(yb.x), bfhi(yb.x), bflo(yb.y), bfhi(yb.y)}; f32x4 ov;
; #pragma unroll
;         for (int r = 0; r < 4; ++r) ov[r] = gelu_tanh(yg[r]) * (hl[r] + a[r] * hi4[r]);
;         *(u32x2*)(mixed + (size_t)(t0 + t) * D + RW + cb + c4) = pack4(ov); }
	v_lshlrev_b32_e32 v30, 16, v52
	v_and_b32_e32 v31, 0xffff0000, v52
	v_lshlrev_b32_e32 v28, 16, v50
	v_pk_add_f32 v[26:27], v[26:27], 1.0 op_sel_hi:[1,0]
	v_and_b32_e32 v29, 0xffff0000, v50
	v_div_scale_f32 v18, s[6:7], v27, v27, 2.0
	v_rcp_f32_e32 v32, v18
	v_pk_mul_f32 v[24:25], v[24:25], 0.5 op_sel_hi:[1,0]
	v_pk_fma_f32 v[28:29], v[0:1], v[28:29], v[30:31]
	v_fma_f32 v20, -v18, v32, 1.0
	v_fmac_f32_e32 v32, v20, v32
	v_div_scale_f32 v20, vcc, 2.0, v27, 2.0
	v_mul_f32_e32 v22, v20, v32
	v_fma_f32 v33, -v18, v22, v20
	v_fmac_f32_e32 v22, v33, v32
	v_fma_f32 v18, -v18, v22, v20
	v_div_scale_f32 v20, s[6:7], v26, v26, 2.0
	v_rcp_f32_e32 v33, v20
	v_div_fmas_f32 v18, v18, v32, v22
	v_div_fixup_f32 v27, v18, v27, 2.0
	v_fma_f32 v18, -v20, v33, 1.0
	v_fmac_f32_e32 v33, v18, v33
	v_div_scale_f32 v18, vcc, 2.0, v26, 2.0
	v_mul_f32_e32 v22, v18, v33
	v_fma_f32 v32, -v20, v22, v18
	v_fmac_f32_e32 v22, v32, v33
	v_fma_f32 v18, -v20, v22, v18
	v_div_fmas_f32 v18, v18, v33, v22
	v_div_fixup_f32 v26, v18, v26, 2.0
	v_lshlrev_b32_e32 v18, 16, v55
	v_mul_f32_e32 v20, 0x3d372713, v18
	v_mul_f32_e32 v20, v20, v18
	v_mov_b32_e32 v22, v18
	v_fmac_f32_e32 v22, v20, v22
	v_mul_f32_e32 v20, 0x3f4c422a, v22
	v_pk_add_f32 v[26:27], v[26:27], 1.0 op_sel_hi:[1,0] neg_lo:[1,0] neg_hi:[1,0]
	v_add_f32_e32 v20, v20, v20
	v_pk_add_f32 v[26:27], v[26:27], 1.0 op_sel_hi:[1,0]
	v_and_b32_e32 v19, 0xffff0000, v55
	v_mul_f32_e32 v20, 0x3fb8aa3b, v20
	v_pk_mul_f32 v[24:25], v[24:25], v[26:27]
	v_exp_f32_e32 v26, v20
	v_mul_f32_e32 v20, 0x3d372713, v19
	v_mul_f32_e32 v20, v20, v19
	v_mov_b32_e32 v22, v19
	v_fmac_f32_e32 v22, v20, v22
	v_mul_f32_e32 v20, 0x3f4c422a, v22
	v_add_f32_e32 v20, v20, v20
	v_mul_f32_e32 v20, 0x3fb8aa3b, v20
	v_exp_f32_e32 v27, v20
	v_pk_mul_f32 v[24:25], v[28:29], v[24:25]
	v_lshlrev_b32_e32 v22, 16, v51
	v_and_b32_e32 v23, 0xffff0000, v51
	v_pk_add_f32 v[26:27], v[26:27], 1.0 op_sel_hi:[1,0]
	v_lshlrev_b32_e32 v20, 16, v53
	v_div_scale_f32 v28, s[6:7], v27, v27, 2.0
	v_rcp_f32_e32 v29, v28
	v_and_b32_e32 v21, 0xffff0000, v53
	v_pk_mul_f32 v[18:19], v[18:19], 0.5 op_sel_hi:[1,0]
	v_pk_fma_f32 v[20:21], v[2:3], v[22:23], v[20:21]
	v_fma_f32 v30, -v28, v29, 1.0
	v_fmac_f32_e32 v29, v30, v29
	v_div_scale_f32 v30, vcc, 2.0, v27, 2.0
	v_mul_f32_e32 v31, v30, v29
	v_fma_f32 v32, -v28, v31, v30
	v_fmac_f32_e32 v31, v32, v29
	v_fma_f32 v28, -v28, v31, v30
	v_div_scale_f32 v30, s[6:7], v26, v26, 2.0
	v_rcp_f32_e32 v32, v30
	v_div_fmas_f32 v28, v28, v29, v31
	v_div_fixup_f32 v27, v28, v27, 2.0
	v_fma_f32 v28, -v30, v32, 1.0
	v_fmac_f32_e32 v32, v28, v32
	v_div_scale_f32 v28, vcc, 2.0, v26, 2.0
	v_mul_f32_e32 v29, v28, v32
	v_fma_f32 v31, -v30, v29, v28
	v_fmac_f32_e32 v29, v31, v32
	v_fma_f32 v28, -v30, v29, v28
	v_div_fmas_f32 v28, v28, v32, v29
	v_sub_co_u32_e32 v14, vcc, 0, v14
	v_div_fixup_f32 v26, v28, v26, 2.0
	s_nop 0
	v_subb_co_u32_e32 v15, vcc, 0, v15, vcc
	v_pk_add_f32 v[26:27], v[26:27], 1.0 op_sel_hi:[1,0] neg_lo:[1,0] neg_hi:[1,0]
	v_lshl_add_u64 v[14:15], v[16:17], 0, v[14:15]
	v_pk_add_f32 v[26:27], v[26:27], 1.0 op_sel_hi:[1,0]
	v_lshl_add_u64 v[14:15], v[14:15], 0, v[8:9]
	v_pk_mul_f32 v[18:19], v[18:19], v[26:27]
	v_lshl_add_u64 v[14:15], v[14:15], 0, v[4:5]
	v_pk_mul_f32 v[18:19], v[20:21], v[18:19]
	v_add_co_u32_e32 v14, vcc, s61, v14
	v_cvt_pk_bf16_f32 v19, v18, v19
	v_cvt_pk_bf16_f32 v18, v24, v25
	v_addc_co_u32_e32 v15, vcc, 0, v15, vcc
	global_store_dwordx2 v[14:15], v[18:19], off offset:2048
	v_add_u32_e32 v14, 0xa00, v6
	v_ashrrev_i32_e32 v14, 5, v14
	v_add_u32_e32 v14, s8, v14
	v_mad_i64_i32 v[16:17], s[6:7], v14, s59, v[12:13]
	v_lshl_add_u64 v[18:19], v[16:17], 0, v[8:9]
	v_lshl_add_u64 v[18:19], v[18:19], 0, v[4:5]
	v_add_co_u32_e32 v18, vcc, s60, v18
	v_ashrrev_i32_e32 v15, 31, v14
	s_nop 0
	v_addc_co_u32_e32 v19, vcc, 0, v19, vcc
	v_lshl_add_u64 v[48:49], v[48:49], 0, v[64:65]
	global_load_dwordx2 v[54:55], v[48:49], off offset:2048
	v_lshl_add_u64 v[44:45], v[44:45], 0, v[62:63]
	global_load_dwordx2 v[50:51], v[44:45], off
	v_lshl_add_u64 v[46:47], v[46:47], 0, v[62:63]
	global_load_dwordx2 v[52:53], v[46:47], off
	v_lshlrev_b64 v[20:21], 10, v[14:15]
	v_or_b32_e32 v20, v20, v7
	v_lshl_add_u64 v[20:21], v[10:11], 0, v[20:21]
	v_lshlrev_b64 v[20:21], 1, v[20:21]
	v_lshl_add_u64 v[22:23], s[38:39], 0, v[20:21]
	v_lshl_add_u64 v[20:21], s[48:49], 0, v[20:21]
	v_lshlrev_b64 v[14:15], 13, v[14:15]
	s_waitcnt vmcnt(6)
	v_lshlrev_b32_e32 v24, 16, v60
	v_and_b32_e32 v25, 0xffff0000, v60
	v_mul_f32_e32 v18, 0x3d372713, v24
	v_mul_f32_e32 v18, v18, v24
	v_mov_b32_e32 v26, v24
	v_fmac_f32_e32 v26, v18, v26
	v_mul_f32_e32 v18, 0x3f4c422a, v26
	v_add_f32_e32 v18, v18, v18
	v_mul_f32_e32 v18, 0x3fb8aa3b, v18
	v_exp_f32_e32 v26, v18
	v_mul_f32_e32 v18, 0x3d372713, v25
	v_mul_f32_e32 v18, v18, v25
	v_mov_b32_e32 v27, v25
	v_fmac_f32_e32 v27, v18, v27
	v_mul_f32_e32 v18, 0x3f4c422a, v27
	v_add_f32_e32 v18, v18, v18
	v_mul_f32_e32 v18, 0x3fb8aa3b, v18
	v_exp_f32_e32 v27, v18
	s_waitcnt vmcnt(4)
; #define LAS __attribute__((address_space(3)))
; DI float bflo(unsigned w) { return __uint_as_float(w << 16); }
; DI float bfhi(unsigned w) { return __uint_as_float(w & 0xffff0000u); }
; DI u32x2 pack4(f32x4 v) { bf16x4_t r = __builtin_convertvector(v, bf16x4_t); return __builtin_bit_cast(u32x2, r); }
; DI float gelu_tanh(float x) { const float u = 0.7978845608028654f * (x + 0.044715f * x * x * x); const float e = __expf(2.0f * u); const float th = 1.0f - 2.0f / (e + 1.0f); return 0.5f * x * (1.0f + th); }
; DI void lru_fin_unit(const Ctx& c, int u) {
;     ...
;     for (int it = 0; it < 8; ++it) { const int item = tid + it * NTHR, t = item >> 5, c4 = (item & 31) * 4;
;         const size_t o = (size_t)(t0 + t) * LW + cb + c4;
;         const u32x2 ar = *(const u32x2*)(acum + o), hr = *(const u32x2*)(hloc + o);
;         const f32x4 a = {bflo(ar.x), bfhi(ar.x), bflo(ar.y), bfhi(ar.y)}, hl = {bflo(hr.x), bfhi(hr.x), bflo(hr.y), bfhi(hr.y)}, hi4 = *(const LAS f32x4*)(hin + c4);
;         const u32x2 yb = *(const u32x2*)(proj + (size_t)(t0 + t) * INC + 5 * RW + cb + c4);
;         const float yg[4] = {bflo(yb.x), bfhi(yb.x), bflo(yb.y), bfhi(yb.y)}; f32x4 ov;
; #pragma unroll
;         for (int r = 0; r < 4; ++r) ov[r] = gelu_tanh(yg[r]) * (hl[r] + a[r] * hi4[r]);
;         *(u32x2*)(mixed + (size_t)(t0 + t) * D + RW + cb + c4) = pack4(ov); }
	v_lshlrev_b32_e32 v30, 16, v58
	v_and_b32_e32 v31, 0xffff0000, v58
	v_lshlrev_b32_e32 v28, 16, v56
	v_pk_add_f32 v[26:27], v[26:27], 1.0 op_sel_hi:[1,0]
	v_and_b32_e32 v29, 0xffff0000, v56
	v_div_scale_f32 v18, s[6:7], v27, v27, 2.0
	v_rcp_f32_e32 v32, v18
	v_pk_mul_f32 v[24:25], v[24:25], 0.5 op_sel_hi:[1,0]
	v_pk_fma_f32 v[28:29], v[0:1], v[28:29], v[30:31]
	v_fma_f32 v20, -v18, v32, 1.0
	v_fmac_f32_e32 v32, v20, v32
	v_div_scale_f32 v20, vcc, 2.0, v27, 2.0
	v_mul_f32_e32 v22, v20, v32
	v_fma_f32 v33, -v18, v22, v20
	v_fmac_f32_e32 v22, v33, v32
	v_fma_f32 v18, -v18, v22, v20
	v_div_scale_f32 v20, s[6:7], v26, v26, 2.0
	v_rcp_f32_e32 v33, v20
	v_div_fmas_f32 v18, v18, v32, v22
	v_div_fixup_f32 v27, v18, v27, 2.0
	v_fma_f32 v18, -v20, v33, 1.0
	v_fmac_f32_e32 v33, v18, v33
	v_div_scale_f32 v18, vcc, 2.0, v26, 2.0
	v_mul_f32_e32 v22, v18, v33
	v_fma_f32 v32, -v20, v22, v18
	v_fmac_f32_e32 v22, v32, v33
	v_fma_f32 v18, -v20, v22, v18
	v_div_fmas_f32 v18, v18, v33, v22
	v_div_fixup_f32 v26, v18, v26, 2.0
	v_lshlrev_b32_e32 v18, 16, v61
	v_mul_f32_e32 v20, 0x3d372713, v18
	v_mul_f32_e32 v20, v20, v18
	v_mov_b32_e32 v22, v18
	v_fmac_f32_e32 v22, v20, v22
	v_mul_f32_e32 v20, 0x3f4c422a, v22
	v_pk_add_f32 v[26:27], v[26:27], 1.0 op_sel_hi:[1,0] neg_lo:[1,0] neg_hi:[1,0]
	v_add_f32_e32 v20, v20, v20
	v_pk_add_f32 v[26:27], v[26:27], 1.0 op_sel_hi:[1,0]
	v_and_b32_e32 v19, 0xffff0000, v61
	v_mul_f32_e32 v20, 0x3fb8aa3b, v20
	v_pk_mul_f32 v[24:25], v[24:25], v[26:27]
	v_exp_f32_e32 v26, v20
	v_mul_f32_e32 v20, 0x3d372713, v19
	v_mul_f32_e32 v20, v20, v19
	v_mov_b32_e32 v22, v19
	v_fmac_f32_e32 v22, v20, v22
	v_mul_f32_e32 v20, 0x3f4c422a, v22
	v_add_f32_e32 v20, v20, v20
	v_mul_f32_e32 v20, 0x3fb8aa3b, v20
	v_exp_f32_e32 v27, v20
	v_pk_mul_f32 v[24:25], v[28:29], v[24:25]
	v_lshlrev_b32_e32 v22, 16, v57
	v_and_b32_e32 v23, 0xffff0000, v57
	v_pk_add_f32 v[26:27], v[26:27], 1.0 op_sel_hi:[1,0]
	v_lshlrev_b32_e32 v20, 16, v59
	v_div_scale_f32 v28, s[6:7], v27, v27, 2.0
	v_rcp_f32_e32 v29, v28
	v_and_b32_e32 v21, 0xffff0000, v59
	v_pk_mul_f32 v[18:19], v[18:19], 0.5 op_sel_hi:[1,0]
	v_pk_fma_f32 v[20:21], v[2:3], v[22:23], v[20:21]
	v_fma_f32 v30, -v28, v29, 1.0
	v_fmac_f32_e32 v29, v30, v29
	v_div_scale_f32 v30, vcc, 2.0, v27, 2.0
	v_mul_f32_e32 v31, v30, v29
	v_fma_f32 v32, -v28, v31, v30
	v_fmac_f32_e32 v31, v32, v29
	v_fma_f32 v28, -v28, v31, v30
	v_div_scale_f32 v30, s[6:7], v26, v26, 2.0
	v_rcp_f32_e32 v32, v30
	v_div_fmas_f32 v28, v28, v29, v31
	v_div_fixup_f32 v27, v28, v27, 2.0
	v_fma_f32 v28, -v30, v32, 1.0
	v_fmac_f32_e32 v32, v28, v32
	v_div_scale_f32 v28, vcc, 2.0, v26, 2.0
	v_mul_f32_e32 v29, v28, v32
	v_fma_f32 v31, -v30, v29, v28
	v_fmac_f32_e32 v29, v31, v32
	v_fma_f32 v28, -v30, v29, v28
	v_div_fmas_f32 v28, v28, v32, v29
	v_sub_co_u32_e32 v14, vcc, 0, v14
	v_div_fixup_f32 v26, v28, v26, 2.0
	s_nop 0
	v_subb_co_u32_e32 v15, vcc, 0, v15, vcc
	v_pk_add_f32 v[26:27], v[26:27], 1.0 op_sel_hi:[1,0] neg_lo:[1,0] neg_hi:[1,0]
	v_lshl_add_u64 v[14:15], v[16:17], 0, v[14:15]
	v_pk_add_f32 v[26:27], v[26:27], 1.0 op_sel_hi:[1,0]
	v_lshl_add_u64 v[14:15], v[14:15], 0, v[8:9]
	v_pk_mul_f32 v[18:19], v[18:19], v[26:27]
	v_lshl_add_u64 v[14:15], v[14:15], 0, v[4:5]
	v_pk_mul_f32 v[18:19], v[20:21], v[18:19]
	v_add_co_u32_e32 v14, vcc, s61, v14
	v_cvt_pk_bf16_f32 v19, v18, v19
	v_cvt_pk_bf16_f32 v18, v24, v25
	v_addc_co_u32_e32 v15, vcc, 0, v15, vcc
	global_store_dwordx2 v[14:15], v[18:19], off offset:2048
	v_add_u32_e32 v14, 0xc00, v6
	v_ashrrev_i32_e32 v14, 5, v14
	v_add_u32_e32 v14, s8, v14
	v_mad_i64_i32 v[16:17], s[6:7], v14, s59, v[12:13]
	v_lshl_add_u64 v[18:19], v[16:17], 0, v[8:9]
	v_lshl_add_u64 v[18:19], v[18:19], 0, v[4:5]
	v_add_co_u32_e32 v18, vcc, s60, v18
	v_ashrrev_i32_e32 v15, 31, v14
	s_nop 0
	v_addc_co_u32_e32 v19, vcc, 0, v19, vcc
	v_lshl_add_u64 v[48:49], v[48:49], 0, v[64:65]
	global_load_dwordx2 v[60:61], v[48:49], off offset:2048
	v_lshl_add_u64 v[44:45], v[44:45], 0, v[62:63]
	global_load_dwordx2 v[56:57], v[44:45], off
	v_lshl_add_u64 v[46:47], v[46:47], 0, v[62:63]
	global_load_dwordx2 v[58:59], v[46:47], off
	v_lshlrev_b64 v[20:21], 10, v[14:15]
	v_or_b32_e32 v20, v20, v7
	v_lshl_add_u64 v[20:21], v[10:11], 0, v[20:21]
	v_lshlrev_b64 v[20:21], 1, v[20:21]
	v_lshl_add_u64 v[22:23], s[38:39], 0, v[20:21]
	v_lshl_add_u64 v[20:21], s[48:49], 0, v[20:21]
	v_lshlrev_b64 v[14:15], 13, v[14:15]
	v_add_u32_e32 v6, 0xe00, v6
	v_ashrrev_i32_e32 v6, 5, v6
	s_waitcnt vmcnt(6)
	v_lshlrev_b32_e32 v24, 16, v54
	v_and_b32_e32 v25, 0xffff0000, v54
	v_mul_f32_e32 v18, 0x3d372713, v24
	v_mul_f32_e32 v18, v18, v24
	v_mov_b32_e32 v26, v24
	v_fmac_f32_e32 v26, v18, v26
	v_mul_f32_e32 v18, 0x3f4c422a, v26
	v_add_f32_e32 v18, v18, v18
	v_mul_f32_e32 v18, 0x3fb8aa3b, v18
	v_exp_f32_e32 v26, v18
	v_mul_f32_e32 v18, 0x3d372713, v25
	v_mul_f32_e32 v18, v18, v25
	v_mov_b32_e32 v27, v25
	v_fmac_f32_e32 v27, v18, v27
	v_mul_f32_e32 v18, 0x3f4c422a, v27
	v_add_f32_e32 v18, v18, v18
	v_mul_f32_e32 v18, 0x3fb8aa3b, v18
	v_exp_f32_e32 v27, v18
	s_waitcnt vmcnt(4)
; #define LAS __attribute__((address_space(3)))
; DI float bflo(unsigned w) { return __uint_as_float(w << 16); }
; DI float bfhi(unsigned w) { return __uint_as_float(w & 0xffff0000u); }
; DI u32x2 pack4(f32x4 v) { bf16x4_t r = __builtin_convertvector(v, bf16x4_t); return __builtin_bit_cast(u32x2, r); }
; DI float gelu_tanh(float x) { const float u = 0.7978845608028654f * (x + 0.044715f * x * x * x); const float e = __expf(2.0f * u); const float th = 1.0f - 2.0f / (e + 1.0f); return 0.5f * x * (1.0f + th); }
; DI void lru_fin_unit(const Ctx& c, int u) {
;     ...
;     for (int it = 0; it < 8; ++it) { const int item = tid + it * NTHR, t = item >> 5, c4 = (item & 31) * 4;
;         const size_t o = (size_t)(t0 + t) * LW + cb + c4;
;         const u32x2 ar = *(const u32x2*)(acum + o), hr = *(const u32x2*)(hloc + o);
;         const f32x4 a = {bflo(ar.x), bfhi(ar.x), bflo(ar.y), bfhi(ar.y)}, hl = {bflo(hr.x), bfhi(hr.x), bflo(hr.y), bfhi(hr.y)}, hi4 = *(const LAS f32x4*)(hin + c4);
;         const u32x2 yb = *(const u32x2*)(proj + (size_t)(t0 + t) * INC + 5 * RW + cb + c4);
;         const float yg[4] = {bflo(yb.x), bfhi(yb.x), bflo(yb.y), bfhi(yb.y)}; f32x4 ov;
; #pragma unroll
;         for (int r = 0; r < 4; ++r) ov[r] = gelu_tanh(yg[r]) * (hl[r] + a[r] * hi4[r]);
;         *(u32x2*)(mixed + (size_t)(t0 + t) * D + RW + cb + c4) = pack4(ov); }
	v_lshlrev_b32_e32 v30, 16, v52
	v_and_b32_e32 v31, 0xffff0000, v52
	v_lshlrev_b32_e32 v28, 16, v50
	v_pk_add_f32 v[26:27], v[26:27], 1.0 op_sel_hi:[1,0]
	v_and_b32_e32 v29, 0xffff0000, v50
	v_div_scale_f32 v18, s[6:7], v27, v27, 2.0
	v_rcp_f32_e32 v32, v18
	v_pk_mul_f32 v[24:25], v[24:25], 0.5 op_sel_hi:[1,0]
	v_pk_fma_f32 v[28:29], v[0:1], v[28:29], v[30:31]
	v_fma_f32 v20, -v18, v32, 1.0
	v_fmac_f32_e32 v32, v20, v32
	v_div_scale_f32 v20, vcc, 2.0, v27, 2.0
	v_mul_f32_e32 v22, v20, v32
	v_fma_f32 v33, -v18, v22, v20
	v_fmac_f32_e32 v22, v33, v32
	v_fma_f32 v18, -v18, v22, v20
	v_div_scale_f32 v20, s[6:7], v26, v26, 2.0
	v_rcp_f32_e32 v33, v20
	v_div_fmas_f32 v18, v18, v32, v22
	v_div_fixup_f32 v27, v18, v27, 2.0
	v_fma_f32 v18, -v20, v33, 1.0
	v_fmac_f32_e32 v33, v18, v33
	v_div_scale_f32 v18, vcc, 2.0, v26, 2.0
	v_mul_f32_e32 v22, v18, v33
	v_fma_f32 v32, -v20, v22, v18
	v_fmac_f32_e32 v22, v32, v33
	v_fma_f32 v18, -v20, v22, v18
	v_div_fmas_f32 v18, v18, v33, v22
	v_div_fixup_f32 v26, v18, v26, 2.0
	v_lshlrev_b32_e32 v18, 16, v55
	v_mul_f32_e32 v20, 0x3d372713, v18
	v_mul_f32_e32 v20, v20, v18
	v_mov_b32_e32 v22, v18
	v_fmac_f32_e32 v22, v20, v22
	v_mul_f32_e32 v20, 0x3f4c422a, v22
	v_pk_add_f32 v[26:27], v[26:27], 1.0 op_sel_hi:[1,0] neg_lo:[1,0] neg_hi:[1,0]
	v_add_f32_e32 v20, v20, v20
	v_pk_add_f32 v[26:27], v[26:27], 1.0 op_sel_hi:[1,0]
	v_and_b32_e32 v19, 0xffff0000, v55
	v_mul_f32_e32 v20, 0x3fb8aa3b, v20
	v_pk_mul_f32 v[24:25], v[24:25], v[26:27]
	v_exp_f32_e32 v26, v20
	v_mul_f32_e32 v20, 0x3d372713, v19
	v_mul_f32_e32 v20, v20, v19
	v_mov_b32_e32 v22, v19
	v_fmac_f32_e32 v22, v20, v22
	v_mul_f32_e32 v20, 0x3f4c422a, v22
	v_add_f32_e32 v20, v20, v20
	v_mul_f32_e32 v20, 0x3fb8aa3b, v20
	v_exp_f32_e32 v27, v20
	v_pk_mul_f32 v[24:25], v[28:29], v[24:25]
	v_lshlrev_b32_e32 v22, 16, v51
	v_and_b32_e32 v23, 0xffff0000, v51
	v_pk_add_f32 v[26:27], v[26:27], 1.0 op_sel_hi:[1,0]
	v_lshlrev_b32_e32 v20, 16, v53
	v_div_scale_f32 v28, s[6:7], v27, v27, 2.0
	v_rcp_f32_e32 v29, v28
	v_and_b32_e32 v21, 0xffff0000, v53
	v_pk_mul_f32 v[18:19], v[18:19], 0.5 op_sel_hi:[1,0]
	v_pk_fma_f32 v[20:21], v[2:3], v[22:23], v[20:21]
	v_fma_f32 v30, -v28, v29, 1.0
	v_fmac_f32_e32 v29, v30, v29
	v_div_scale_f32 v30, vcc, 2.0, v27, 2.0
	v_mul_f32_e32 v31, v30, v29
	v_fma_f32 v32, -v28, v31, v30
	v_fmac_f32_e32 v31, v32, v29
	v_fma_f32 v28, -v28, v31, v30
	v_div_scale_f32 v30, s[6:7], v26, v26, 2.0
	v_rcp_f32_e32 v32, v30
	v_div_fmas_f32 v28, v28, v29, v31
	v_div_fixup_f32 v27, v28, v27, 2.0
	v_fma_f32 v28, -v30, v32, 1.0
	v_fmac_f32_e32 v32, v28, v32
	v_div_scale_f32 v28, vcc, 2.0, v26, 2.0
	v_mul_f32_e32 v29, v28, v32
	v_fma_f32 v31, -v30, v29, v28
	v_fmac_f32_e32 v29, v31, v32
	v_fma_f32 v28, -v30, v29, v28
	v_div_fmas_f32 v28, v28, v32, v29
	v_sub_co_u32_e32 v14, vcc, 0, v14
	v_div_fixup_f32 v26, v28, v26, 2.0
	s_nop 0
	v_subb_co_u32_e32 v15, vcc, 0, v15, vcc
	v_pk_add_f32 v[26:27], v[26:27], 1.0 op_sel_hi:[1,0] neg_lo:[1,0] neg_hi:[1,0]
	v_lshl_add_u64 v[14:15], v[16:17], 0, v[14:15]
	v_pk_add_f32 v[26:27], v[26:27], 1.0 op_sel_hi:[1,0]
	v_lshl_add_u64 v[14:15], v[14:15], 0, v[8:9]
	v_pk_mul_f32 v[18:19], v[18:19], v[26:27]
	v_lshl_add_u64 v[14:15], v[14:15], 0, v[4:5]
	v_pk_mul_f32 v[18:19], v[20:21], v[18:19]
	v_add_co_u32_e32 v14, vcc, s61, v14
	v_cvt_pk_bf16_f32 v19, v18, v19
	v_cvt_pk_bf16_f32 v18, v24, v25
	v_addc_co_u32_e32 v15, vcc, 0, v15, vcc
	global_store_dwordx2 v[14:15], v[18:19], off offset:2048
	v_add_u32_e32 v14, s8, v6
	v_mad_i64_i32 v[12:13], s[6:7], v14, s59, v[12:13]
	v_lshl_add_u64 v[16:17], v[12:13], 0, v[8:9]
	v_lshl_add_u64 v[16:17], v[16:17], 0, v[4:5]
	v_add_co_u32_e32 v16, vcc, s60, v16
	v_ashrrev_i32_e32 v15, 31, v14
	s_nop 0
	v_addc_co_u32_e32 v17, vcc, 0, v17, vcc
	v_lshlrev_b64 v[18:19], 10, v[14:15]
	v_or_b32_e32 v18, v18, v7
	v_lshl_add_u64 v[6:7], v[10:11], 0, v[18:19]
	v_lshlrev_b64 v[6:7], 1, v[6:7]
	v_lshl_add_u64 v[10:11], s[38:39], 0, v[6:7]
	v_lshl_add_u64 v[6:7], s[48:49], 0, v[6:7]
	s_waitcnt vmcnt(3)
; #define LAS __attribute__((address_space(3)))
; DI float bflo(unsigned w) { return __uint_as_float(w << 16); }
; DI float bfhi(unsigned w) { return __uint_as_float(w & 0xffff0000u); }
; DI u32x2 pack4(f32x4 v) { bf16x4_t r = __builtin_convertvector(v, bf16x4_t); return __builtin_bit_cast(u32x2, r); }
; DI float gelu_tanh(float x) { const float u = 0.7978845608028654f * (x + 0.044715f * x * x * x); const float e = __expf(2.0f * u); const float th = 1.0f - 2.0f / (e + 1.0f); return 0.5f * x * (1.0f + th); }
; DI void lru_fin_unit(const Ctx& c, int u) {
;     ...
;     for (int it = 0; it < 8; ++it) { const int item = tid + it * NTHR, t = item >> 5, c4 = (item & 31) * 4;
;         const size_t o = (size_t)(t0 + t) * LW + cb + c4;
;         const u32x2 ar = *(const u32x2*)(acum + o), hr = *(const u32x2*)(hloc + o);
;         const f32x4 a = {bflo(ar.x), bfhi(ar.x), bflo(ar.y), bfhi(ar.y)}, hl = {bflo(hr.x), bfhi(hr.x), bflo(hr.y), bfhi(hr.y)}, hi4 = *(const LAS f32x4*)(hin + c4);
;         const u32x2 yb = *(const u32x2*)(proj + (size_t)(t0 + t) * INC + 5 * RW + cb + c4);
;         const float yg[4] = {bflo(yb.x), bfhi(yb.x), bflo(yb.y), bfhi(yb.y)}; f32x4 ov;
; #pragma unroll
;         for (int r = 0; r < 4; ++r) ov[r] = gelu_tanh(yg[r]) * (hl[r] + a[r] * hi4[r]);
;         *(u32x2*)(mixed + (size_t)(t0 + t) * D + RW + cb + c4) = pack4(ov); }
	v_lshlrev_b32_e32 v18, 16, v60
	v_and_b32_e32 v19, 0xffff0000, v60
	v_mul_f32_e32 v16, 0x3d372713, v18
	v_mul_f32_e32 v16, v16, v18
	v_mov_b32_e32 v20, v18
	v_fmac_f32_e32 v20, v16, v20
	v_mul_f32_e32 v16, 0x3f4c422a, v20
	v_add_f32_e32 v16, v16, v16
	v_mul_f32_e32 v16, 0x3fb8aa3b, v16
	v_exp_f32_e32 v20, v16
	v_mul_f32_e32 v16, 0x3d372713, v19
	v_mul_f32_e32 v16, v16, v19
	v_mov_b32_e32 v21, v19
	v_fmac_f32_e32 v21, v16, v21
	v_mul_f32_e32 v16, 0x3f4c422a, v21
	v_add_f32_e32 v16, v16, v16
	v_mul_f32_e32 v16, 0x3fb8aa3b, v16
	v_exp_f32_e32 v21, v16
	s_waitcnt vmcnt(2)
	v_lshlrev_b32_e32 v22, 16, v56
	v_and_b32_e32 v23, 0xffff0000, v56
	v_pk_mul_f32 v[18:19], v[18:19], 0.5 op_sel_hi:[1,0]
	v_pk_add_f32 v[20:21], v[20:21], 1.0 op_sel_hi:[1,0]
	s_waitcnt vmcnt(1)
	v_lshlrev_b32_e32 v24, 16, v58
	v_div_scale_f32 v16, s[6:7], v21, v21, 2.0
	v_rcp_f32_e32 v26, v16
	v_and_b32_e32 v25, 0xffff0000, v58
	v_pk_fma_f32 v[0:1], v[0:1], v[22:23], v[24:25]
	v_fma_f32 v6, -v16, v26, 1.0
	v_fmac_f32_e32 v26, v6, v26
	v_div_scale_f32 v6, vcc, 2.0, v21, 2.0
	v_mul_f32_e32 v10, v6, v26
	v_fma_f32 v27, -v16, v10, v6
	v_fmac_f32_e32 v10, v27, v26
	v_fma_f32 v6, -v16, v10, v6
	v_div_scale_f32 v16, s[6:7], v20, v20, 2.0
	v_rcp_f32_e32 v27, v16
	v_div_fmas_f32 v6, v6, v26, v10
	v_div_fixup_f32 v21, v6, v21, 2.0
	v_fma_f32 v6, -v16, v27, 1.0
	v_fmac_f32_e32 v27, v6, v27
	v_div_scale_f32 v6, vcc, 2.0, v20, 2.0
	v_mul_f32_e32 v10, v6, v27
	v_fma_f32 v26, -v16, v10, v6
	v_fmac_f32_e32 v10, v26, v27
	v_fma_f32 v6, -v16, v10, v6
	v_div_fmas_f32 v6, v6, v27, v10
	v_lshlrev_b32_e32 v16, 16, v61
	v_div_fixup_f32 v20, v6, v20, 2.0
	v_mul_f32_e32 v6, 0x3d372713, v16
	v_mul_f32_e32 v6, v6, v16
	v_mov_b32_e32 v10, v16
	v_fmac_f32_e32 v10, v6, v10
	v_mul_f32_e32 v6, 0x3f4c422a, v10
	v_pk_add_f32 v[20:21], v[20:21], 1.0 op_sel_hi:[1,0] neg_lo:[1,0] neg_hi:[1,0]
	v_add_f32_e32 v6, v6, v6
	v_pk_add_f32 v[20:21], v[20:21], 1.0 op_sel_hi:[1,0]
	v_and_b32_e32 v17, 0xffff0000, v61
	v_mul_f32_e32 v6, 0x3fb8aa3b, v6
	v_pk_mul_f32 v[18:19], v[18:19], v[20:21]
	v_exp_f32_e32 v20, v6
	v_mul_f32_e32 v6, 0x3d372713, v17
	v_mul_f32_e32 v6, v6, v17
	v_mov_b32_e32 v10, v17
	v_fmac_f32_e32 v10, v6, v10
	v_mul_f32_e32 v6, 0x3f4c422a, v10
	v_add_f32_e32 v6, v6, v6
	v_mul_f32_e32 v6, 0x3fb8aa3b, v6
	v_exp_f32_e32 v21, v6
	v_pk_mul_f32 v[0:1], v[0:1], v[18:19]
	v_lshlrev_b32_e32 v10, 16, v57
	v_and_b32_e32 v11, 0xffff0000, v57
	v_pk_add_f32 v[18:19], v[20:21], 1.0 op_sel_hi:[1,0]
	v_lshlrev_b32_e32 v6, 16, v59
	v_div_scale_f32 v20, s[6:7], v19, v19, 2.0
	v_rcp_f32_e32 v21, v20
	v_and_b32_e32 v7, 0xffff0000, v59
	v_pk_mul_f32 v[16:17], v[16:17], 0.5 op_sel_hi:[1,0]
	v_pk_fma_f32 v[2:3], v[2:3], v[10:11], v[6:7]
	v_fma_f32 v22, -v20, v21, 1.0
	v_fmac_f32_e32 v21, v22, v21
	v_div_scale_f32 v22, vcc, 2.0, v19, 2.0
	v_mul_f32_e32 v23, v22, v21
	v_fma_f32 v24, -v20, v23, v22
	v_fmac_f32_e32 v23, v24, v21
	v_fma_f32 v20, -v20, v23, v22
	v_div_scale_f32 v22, s[6:7], v18, v18, 2.0
	v_rcp_f32_e32 v24, v22
	v_div_fmas_f32 v20, v20, v21, v23
	v_div_fixup_f32 v19, v20, v19, 2.0
	v_fma_f32 v20, -v22, v24, 1.0
	v_fmac_f32_e32 v24, v20, v24
	v_div_scale_f32 v20, vcc, 2.0, v18, 2.0
	v_mul_f32_e32 v21, v20, v24
	v_fma_f32 v23, -v22, v21, v20
	v_fmac_f32_e32 v21, v23, v24
	v_fma_f32 v20, -v22, v21, v20
	v_div_fmas_f32 v20, v20, v24, v21
	v_div_fixup_f32 v18, v20, v18, 2.0
	v_pk_add_f32 v[18:19], v[18:19], 1.0 op_sel_hi:[1,0] neg_lo:[1,0] neg_hi:[1,0]
	s_nop 0
	v_pk_add_f32 v[18:19], v[18:19], 1.0 op_sel_hi:[1,0]
	s_nop 0
	v_pk_mul_f32 v[16:17], v[16:17], v[18:19]
	s_nop 0
	v_pk_mul_f32 v[2:3], v[2:3], v[16:17]
	s_nop 0
	v_cvt_pk_bf16_f32 v3, v2, v3
	v_cvt_pk_bf16_f32 v2, v0, v1
	v_lshlrev_b64 v[0:1], 13, v[14:15]
	v_sub_co_u32_e32 v0, vcc, 0, v0
	s_nop 1
	v_subb_co_u32_e32 v1, vcc, 0, v1, vcc
	v_lshl_add_u64 v[0:1], v[12:13], 0, v[0:1]
	v_lshl_add_u64 v[0:1], v[0:1], 0, v[8:9]
	v_lshl_add_u64 v[0:1], v[0:1], 0, v[4:5]
	v_add_co_u32_e32 v0, vcc, 0x10690000, v0
	s_nop 1
	v_addc_co_u32_e32 v1, vcc, 0, v1, vcc
	global_store_dwordx2 v[0:1], v[2:3], off offset:2048
	s_cbranch_scc1 .LBB0_321
